# v51 + MoE unit schedule: expert lookup by one per-lane LDS read + ballot popcount (was 16 serial LDS reads + 31 compare/add steps per unit)
# speedup vs baseline: 1.0203x; 1.0083x over previous
.LBB0_576:
	s_add_i32 s2, 0, 0x20480
	s_waitcnt lgkmcnt(0)
	v_mov_b32_e32 v0, s2
	s_waitcnt vmcnt(0)
	s_barrier
	ds_read_b32 v0, v0
	s_and_b32 s2, s97, 0xffffffc0
	v_add_u32_e32 v194, s2, v4
	s_waitcnt lgkmcnt(0)
	v_readfirstlane_b32 s2, v0
	s_lshl_b32 s23, s2, 3
	s_cmp_ge_i32 s88, s23
	v_readfirstlane_b32 s2, v194
	s_cbranch_scc1 .LBB0_599
	s_add_u32 s25, s8, 0x12200000
	s_addc_u32 s33, s9, 0
	s_add_u32 s42, s8, 0x2000000
	s_addc_u32 s43, s9, 0
	s_ashr_i32 s4, s2, 6
	s_ashr_i32 s3, s2, 8
	s_lshl_b32 s44, s4, 10
	s_add_u32 s10, s8, 0xe000000
	s_addc_u32 s11, s9, 0
	s_add_i32 s45, 0, 0x20404
	s_ashr_i32 s5, s88, 31
	s_lshr_b32 s5, s5, 29
	s_add_i32 s46, 0, 0x2040c
	s_add_i32 s47, 0, 0x20414
	s_add_i32 s48, 0, 0x2041c
	s_add_i32 s5, s88, s5
	s_ashr_i32 s83, s5, 3
	s_add_i32 s49, 0, 0x20424
	s_add_i32 s50, 0, 0x2042c
	s_add_i32 s51, 0, 0x20434
	s_add_i32 s52, 0, 0x2043c
	s_add_i32 s53, 0, 0x20444
	s_add_i32 s54, 0, 0x2044c
	s_add_i32 s55, 0, 0x20454
	s_add_i32 s56, 0, 0x2045c
	s_add_i32 s57, 0, 0x20464
	s_add_i32 s58, 0, 0x2046c
	s_add_i32 s59, 0, 0x20474
	s_add_i32 s60, 0, 0x2047c
	s_and_b32 s5, s5, -8
	s_sub_i32 s84, s88, s5
	v_ashrrev_i32_e32 v5, 3, v194
	v_add_u32_e32 v10, 64, v5
	v_mov_b32_e32 v165, 0
	v_mov_b32_e32 v161, v165
	v_mov_b32_e32 v163, v165
	s_mov_b32 s85, 0
	v_mov_b32_e32 v173, v165
	s_nop 0
	s_nop 0
	s_nop 1
	s_nop 0
	s_nop 0
	s_nop 1
	s_nop 0
	s_nop 1
	s_nop 1
	s_nop 1
	v_add_u32_e32 v8, 0xc0, v5
	s_nop 0
	s_nop 1
	s_nop 1
	v_add_u32_e32 v6, 0x80, v5
	s_nop 0
	s_nop 1
	s_nop 1
	s_nop 0
	v_mbcnt_lo_u32_b32 v0, -1, 0
	v_mbcnt_hi_u32_b32 v0, -1, v0
	v_lshlrev_b32_e32 v0, 2, v0
	v_add_u32_e32 v0, 0x20400, v0
	ds_read_b32 v0, v0
	s_waitcnt lgkmcnt(0)
	v_cmp_ge_i32_e32 vcc, s83, v0
	s_and_b32 s36, vcc_lo, 0xfffffffe
	s_bcnt1_i32_b32 s36, s36
	s_lshl_b32 s12, s36, 2
	s_add_i32 s12, s12, 0
	s_add_i32 s13, s12, 0x20400
	v_mov_b32_e32 v0, s13
	ds_read_b32 v0, v0
	s_add_i32 s5, s12, 0x20500
	v_mov_b32_e32 v1, s5
	ds_read_b32 v1, v1
	s_ashr_i32 s37, s36, 31
	s_waitcnt lgkmcnt(1)
	v_readfirstlane_b32 s5, v0
	s_sub_i32 s5, s83, s5
	s_lshl_b32 s12, s5, 8
	s_waitcnt lgkmcnt(0)
	v_readfirstlane_b32 s13, v1
	s_sub_i32 s12, s13, s12
	s_min_i32 s12, s12, 0x100
	s_lshl_b32 s5, s5, 17
	s_add_i32 s12, s12, -1
	s_or_b32 s5, s12, s5
	s_and_b32 s14, s12, 0x1ff
	s_ashr_i32 s5, s5, 9
	v_min_i32_e32 v0, s14, v5
	s_lshl_b64 s[12:13], s[36:37], 17
	v_min_i32_e32 v2, s14, v10
	v_add_u32_e32 v0, s5, v0
	s_add_u32 s12, s25, s12
	v_add_u32_e32 v2, s5, v2
	v_min_i32_e32 v6, s14, v6
	v_min_i32_e32 v8, s14, v8
	v_ashrrev_i32_e32 v1, 31, v0
	s_addc_u32 s13, s33, s13
	v_ashrrev_i32_e32 v3, 31, v2
	v_add_u32_e32 v6, s5, v6
	v_add_u32_e32 v8, s5, v8
	v_lshl_add_u64 v[0:1], v[0:1], 2, s[12:13]
	v_lshl_add_u64 v[2:3], v[2:3], 2, s[12:13]
	v_ashrrev_i32_e32 v7, 31, v6
	v_ashrrev_i32_e32 v9, 31, v8
	v_lshl_add_u64 v[6:7], v[6:7], 2, s[12:13]
	v_lshl_add_u64 v[8:9], v[8:9], 2, s[12:13]
	global_load_dword v0, v[0:1], off
	s_nop 0
	global_load_dword v1, v[2:3], off
	s_nop 0
	global_load_dword v2, v[6:7], off
	global_load_dword v3, v[8:9], off
	v_lshrrev_b32_e32 v6, 4, v194
	s_lshl_b32 s12, s84, 7
	v_and_b32_e32 v8, 4, v6
	v_lshrrev_b32_e32 v9, 3, v194
	s_ashr_i32 s13, s12, 31
	v_and_or_b32 v8, v9, 2, v8
	v_lshrrev_b32_e32 v9, 5, v4
	v_lshrrev_b32_e32 v10, 6, v194
	s_lshl_b64 s[14:15], s[36:37], 21
	s_lshl_b64 s[12:13], s[12:13], 10
	v_and_b32_e32 v7, 7, v4
	v_bitop3_b32 v9, v10, 1, v9 bitop3:0x48
	s_add_u32 s5, s42, s14
	v_bitop3_b32 v7, v8, v7, v9 bitop3:0x36
	v_lshrrev_b32_e32 v8, 2, v5
	v_lshlrev_b32_e32 v9, 1, v5
	s_addc_u32 s14, s43, s15
	v_lshlrev_b32_e32 v195, 4, v7
	v_and_b32_e32 v7, 0x3fffe3, v5
	v_and_b32_e32 v8, 4, v8
	v_and_b32_e32 v9, 24, v9
	s_add_u32 s38, s5, s12
	v_or3_b32 v7, v7, v8, v9
	s_addc_u32 s39, s14, s13
	s_add_i32 s61, s44, 0
	v_lshl_or_b32 v160, v7, 10, v195
	s_add_i32 m0, s61, 0x10000
	v_add_u32_e32 v162, 0x10000, v160
	global_load_lds_dwordx4 v160, s[38:39]
	s_add_i32 m0, s61, 0x12000
	s_add_u32 s40, s38, 0x100000
	global_load_lds_dwordx4 v162, s[38:39]
	s_addc_u32 s41, s39, 0
	s_add_i32 m0, s61, 0x14000
	s_add_i32 s62, s61, 0x2000
	global_load_lds_dwordx4 v160, s[40:41]
	s_add_i32 m0, s61, 0x16000
	s_add_i32 s63, s61, 0x4000
	global_load_lds_dwordx4 v162, s[40:41]
	s_mov_b32 m0, s61
	s_add_i32 s64, s61, 0x6000
	s_cmp_eq_u32 s3, 1
	s_cselect_b64 s[12:13], -1, 0
	s_cmp_lg_u32 s3, 1
	s_waitcnt vmcnt(0)
	v_lshl_or_b32 v164, v0, 10, v195
	v_lshl_or_b32 v172, v1, 10, v195
	global_load_lds_dwordx4 v164, s[10:11]
	s_mov_b32 m0, s62
	v_lshl_or_b32 v170, v2, 10, v195
	global_load_lds_dwordx4 v172, s[10:11]
	s_mov_b32 m0, s63
	v_lshl_or_b32 v168, v3, 10, v195
	global_load_lds_dwordx4 v170, s[10:11]
	s_mov_b32 m0, s64
	v_lshl_add_u64 v[2:3], s[38:39], 0, v[160:161]
	global_load_lds_dwordx4 v168, s[10:11]
	v_lshl_add_u64 v[0:1], s[38:39], 0, v[162:163]
	s_cbranch_scc1 .LBB0_579
	s_barrier

.LBB0_582:
	s_add_i32 s80, s85, 1
	s_mul_i32 s2, s80, s96
	s_add_i32 s2, s2, s88
	s_cmp_lt_i32 s2, s23
	s_cselect_b64 s[34:35], -1, 0
	s_cmp_ge_i32 s2, s23
	s_cbranch_scc1 .LBB0_584
	s_ashr_i32 s3, s2, 31
	s_lshr_b32 s3, s3, 29
	s_add_i32 s3, s2, s3
	s_ashr_i32 s79, s3, 3
	s_and_b32 s3, s3, -8
	s_sub_i32 s81, s2, s3
	v_mbcnt_lo_u32_b32 v0, -1, 0
	v_mbcnt_hi_u32_b32 v0, -1, v0
	v_lshlrev_b32_e32 v0, 2, v0
	v_add_u32_e32 v0, 0x20400, v0
	ds_read_b32 v0, v0
	s_waitcnt lgkmcnt(0)
	v_cmp_ge_i32_e32 vcc, s79, v0
	s_and_b32 s26, vcc_lo, 0xfffffffe
	s_bcnt1_i32_b32 s26, s26
	s_lshl_b32 s4, s26, 2
	s_add_i32 s4, s4, 0
	s_add_i32 s5, s4, 0x20400
	v_mov_b32_e32 v0, s5
	ds_read_b32 v0, v0
	s_add_i32 s2, s4, 0x20500
	v_mov_b32_e32 v1, s2
	ds_read_b32 v1, v1
	s_waitcnt lgkmcnt(0)
	v_readfirstlane_b32 s2, v0
	s_sub_i32 s2, s79, s2
	s_lshl_b32 s3, s2, 8
	v_readfirstlane_b32 s4, v1
	s_sub_i32 s3, s4, s3
	s_min_i32 s3, s3, 0x100
	s_lshl_b32 s2, s2, 17
	s_add_i32 s3, s3, -1
	s_or_b32 s82, s3, s2

.LBB0_659:
	s_add_i32 s2, 0, 0x20480
	s_waitcnt lgkmcnt(0)
	v_mov_b32_e32 v0, s2
	s_waitcnt vmcnt(0)
	s_barrier
	ds_read_b32 v0, v0
	s_and_b32 s2, s97, 0xffffffc0
	v_add_u32_e32 v198, s2, v4
	s_waitcnt lgkmcnt(0)
	v_readfirstlane_b32 s2, v0
	s_lshl_b32 s23, s2, 2
	s_cmp_ge_i32 s88, s23
	v_readfirstlane_b32 s2, v198
	s_cbranch_scc1 .LBB0_681
	v_lshrrev_b32_e32 v5, 4, v198
	v_and_b32_e32 v1, 4, v5
	v_lshrrev_b32_e32 v2, 3, v198
	v_and_or_b32 v1, v2, 2, v1
	v_lshrrev_b32_e32 v2, 5, v4
	v_lshrrev_b32_e32 v3, 6, v198
	s_add_u32 s25, s6, 0xa000000
	v_ashrrev_i32_e32 v199, 3, v198
	v_and_b32_e32 v0, 7, v4
	v_bitop3_b32 v2, v3, 1, v2 bitop3:0x48
	s_addc_u32 s33, s7, 0
	v_bitop3_b32 v0, v1, v0, v2 bitop3:0x36
	v_lshrrev_b32_e32 v1, 2, v199
	v_lshlrev_b32_e32 v2, 1, v199
	s_add_u32 s8, s6, 0x12c00000
	v_lshlrev_b32_e32 v201, 4, v0
	v_and_b32_e32 v0, 0x3fffe3, v199
	v_and_b32_e32 v1, 4, v1
	v_and_b32_e32 v2, 24, v2
	s_addc_u32 s9, s7, 0
	v_or3_b32 v0, v0, v1, v2
	s_add_i32 s43, 0, 0x20404
	v_lshl_or_b32 v160, v0, 10, v201
	s_ashr_i32 s10, s88, 31
	s_lshr_b32 s10, s10, 30
	s_add_i32 s44, 0, 0x2040c
	s_add_i32 s45, 0, 0x20414
	s_add_i32 s46, 0, 0x2041c
	s_add_i32 s10, s88, s10
	s_ashr_i32 s79, s10, 2
	s_add_i32 s47, 0, 0x20424
	s_add_i32 s48, 0, 0x2042c
	s_add_i32 s49, 0, 0x20434
	s_add_i32 s50, 0, 0x2043c
	s_add_i32 s51, 0, 0x20444
	s_add_i32 s52, 0, 0x2044c
	s_add_i32 s53, 0, 0x20454
	s_add_i32 s54, 0, 0x2045c
	s_add_i32 s55, 0, 0x20464
	s_add_i32 s56, 0, 0x2046c
	s_add_i32 s57, 0, 0x20474
	s_add_i32 s58, 0, 0x2047c
	s_and_b32 s10, s10, -4
	s_sub_i32 s80, s88, s10
	s_lshl_b32 s10, s79, 8
	v_add_u32_e32 v200, 64, v199
	v_add_u32_e32 v202, 0x80, v199
	v_add_u32_e32 v203, 0xc0, v199
	s_ashr_i32 s18, s2, 6
	s_ashr_i32 s3, s2, 8
	s_lshl_b32 s42, s18, 10
	v_add_u32_e32 v162, 0x10000, v160
	v_mov_b32_e32 v165, 0
	v_mov_b32_e32 v161, v165
	v_mov_b32_e32 v163, v165
	s_mov_b32 s81, 0
	v_mov_b32_e32 v171, v165
	s_nop 0
	s_nop 1
	s_nop 0
	s_nop 1
	s_nop 1
	s_nop 1
	s_nop 1
	s_nop 1
	s_nop 1
	s_nop 1
	s_nop 1
	s_nop 1
	s_nop 0
	v_mbcnt_lo_u32_b32 v0, -1, 0
	v_mbcnt_hi_u32_b32 v0, -1, v0
	v_lshlrev_b32_e32 v0, 2, v0
	v_add_u32_e32 v0, 0x20400, v0
	ds_read_b32 v0, v0
	s_waitcnt lgkmcnt(0)
	v_cmp_ge_i32_e32 vcc, s79, v0
	s_and_b32 s36, vcc_lo, 0xfffffffe
	s_bcnt1_i32_b32 s36, s36
	v_add_u32_e32 v0, s10, v199
	v_lshl_or_b32 v164, v0, 10, v201
	v_add_u32_e32 v0, s10, v200
	v_lshl_or_b32 v170, v0, 10, v201
	v_add_u32_e32 v0, s10, v202
	v_lshl_or_b32 v166, v0, 10, v201
	v_add_u32_e32 v0, s10, v203
	s_lshl_b32 s10, s80, 8
	s_ashr_i32 s37, s36, 31
	s_ashr_i32 s11, s10, 31
	s_lshl_b64 s[12:13], s[36:37], 20
	s_lshl_b64 s[10:11], s[10:11], 10
	s_add_u32 s12, s25, s12
	s_addc_u32 s13, s33, s13
	s_add_u32 s34, s12, s10
	s_addc_u32 s35, s13, s11
	s_add_i32 s59, s42, 0
	s_add_i32 m0, s59, 0x10000
	v_lshl_or_b32 v168, v0, 10, v201
	global_load_lds_dwordx4 v160, s[34:35]
	s_add_i32 m0, s59, 0x12000
	s_add_u32 s38, s34, 0x20000
	global_load_lds_dwordx4 v162, s[34:35]
	s_addc_u32 s39, s35, 0
	s_add_i32 m0, s59, 0x14000
	s_add_i32 s60, s59, 0x2000
	global_load_lds_dwordx4 v160, s[38:39]
	s_add_i32 m0, s59, 0x16000
	s_add_i32 s61, s59, 0x4000
	global_load_lds_dwordx4 v162, s[38:39]
	s_mov_b32 m0, s59
	s_add_i32 s62, s59, 0x6000
	global_load_lds_dwordx4 v164, s[8:9]
	s_mov_b32 m0, s60
	s_cmp_eq_u32 s3, 1
	global_load_lds_dwordx4 v170, s[8:9]
	s_mov_b32 m0, s61
	v_lshl_add_u64 v[2:3], s[34:35], 0, v[160:161]
	global_load_lds_dwordx4 v166, s[8:9]
	s_mov_b32 m0, s62
	v_lshl_add_u64 v[0:1], s[34:35], 0, v[162:163]
	global_load_lds_dwordx4 v168, s[8:9]
	s_cselect_b64 s[10:11], -1, 0
	s_cmp_lg_u32 s3, 1
	s_cbranch_scc1 .LBB0_662
	s_barrier

.LBB0_665:
	s_add_i32 s77, s81, 1
	s_mul_i32 s2, s77, s96
	s_add_i32 s2, s2, s88
	s_cmp_lt_i32 s2, s23
	s_cselect_b64 s[28:29], -1, 0
	s_cmp_ge_i32 s2, s23
	s_cbranch_scc1 .LBB0_667
	s_ashr_i32 s3, s2, 31
	s_lshr_b32 s3, s3, 30
	s_add_i32 s3, s2, s3
	s_ashr_i32 s76, s3, 2
	s_and_b32 s3, s3, -4
	s_sub_i32 s78, s2, s3
	v_mbcnt_lo_u32_b32 v0, -1, 0
	v_mbcnt_hi_u32_b32 v0, -1, v0
	v_lshlrev_b32_e32 v0, 2, v0
	v_add_u32_e32 v0, 0x20400, v0
	ds_read_b32 v0, v0
	s_waitcnt lgkmcnt(0)
	v_cmp_ge_i32_e32 vcc, s76, v0
	s_and_b32 s26, vcc_lo, 0xfffffffe
	s_bcnt1_i32_b32 s26, s26
